# grid barrier: only the last-arriving WG of each XCD invalidates the shared L2 (waited before it releases its XCD); the other WGs of that XCD invalidate just their L1
# baseline (speedup 1.0000x reference)
.LBB0_285:
	s_or_b64 exec, exec, s[4:5]
	s_waitcnt vmcnt(0) lgkmcnt(0)
	buffer_inv sc0
	s_waitcnt vmcnt(0)

.LBB0_301:
	s_or_b64 exec, exec, s[0:1]
	v_mov_b32_e32 v0, s23
	v_add_co_u32_e32 v0, vcc, 0x2000, v0
	v_mov_b32_e32 v1, s22
	s_nop 0
	v_addc_co_u32_e32 v1, vcc, 0, v1, vcc
	v_mov_b32_e32 v2, 1
	s_waitcnt vmcnt(0) lgkmcnt(0)
	buffer_inv sc1
	s_waitcnt vmcnt(0)
	flat_atomic_add v[0:1], v2 offset:1024
	s_waitcnt vmcnt(0)

.LBB0_1130:
	s_or_b64 exec, exec, s[6:7]
	s_waitcnt vmcnt(0) lgkmcnt(0)
	buffer_inv sc0
	s_waitcnt vmcnt(0)

.LBB0_1146:
	s_or_b64 exec, exec, s[2:3]
	v_mov_b32_e32 v0, s40
	v_add_co_u32_e32 v0, vcc, 0x2000, v0
	v_mov_b32_e32 v1, s31
	s_nop 0
	v_addc_co_u32_e32 v1, vcc, 0, v1, vcc
	s_waitcnt vmcnt(0) lgkmcnt(0)
	buffer_inv sc1
	s_waitcnt vmcnt(0)
	flat_atomic_add v[0:1], v200 offset:1024
	s_waitcnt vmcnt(0)

.LBB0_1312:
	s_or_b64 exec, exec, s[2:3]
	v_mov_b32_e32 v0, s40
	v_add_co_u32_e32 v0, vcc, 0x2000, v0
	v_mov_b32_e32 v1, s15
	s_nop 0
	v_addc_co_u32_e32 v1, vcc, 0, v1, vcc
	s_waitcnt vmcnt(0) lgkmcnt(0)
	buffer_inv sc1
	s_waitcnt vmcnt(0)
	flat_atomic_add v[0:1], v200 offset:1024
	s_waitcnt vmcnt(0)

.LBB0_2862:
	s_or_b64 exec, exec, s[2:3]
	v_mov_b32_e32 v0, s31
	v_add_co_u32_e32 v0, vcc, 0x2000, v0
	v_mov_b32_e32 v1, s15
	s_nop 0
	v_addc_co_u32_e32 v1, vcc, 0, v1, vcc
	s_waitcnt vmcnt(0) lgkmcnt(0)
	buffer_inv sc1
	s_waitcnt vmcnt(0)
	flat_atomic_add v[0:1], v200 offset:1024
	s_waitcnt vmcnt(0)
